# v84 + pipelined ticket draw in the P8 quota quantizer loop only (fixed per-workgroup quota, so no tail imbalance)
# baseline (speedup 1.0000x reference)
; #define LAS __attribute__((address_space(3)))
; #define Q_GRAB() (((stop != nullptr && xb_ld(stop) >= thr) || (quota > 0 && qleft-- <= 0)) ? (unsigned)hi : (unsigned)lo + atomicAdd(cnt, 1u))
;     ...
;         unsigned nxt = 0u; if (tid == 0) nxt = Q_GRAB();
;         signed char* Qc = Qp; float* csc = csp; const bool f8c = f8; const float qmax = f8c ? 448.0f : 127.0f, qinv = f8c ? (1.0f / 448.0f) : (1.0f / 127.0f);
;         f32x4 mx = {0.f, 0.f, 0.f, 0.f};
; #pragma unroll
;         for (int g = 0; g < 8; ++g)
; #pragma unroll
;             for (int r = 0; r < 4; ++r) { mx[0] = fmaxf(mx[0], fabsf(v[g][r][0])); mx[1] = fmaxf(mx[1], fabsf(v[g][r][1])); mx[2] = fmaxf(mx[2], fabsf(v[g][r][2])); mx[3] = fmaxf(mx[3], fabsf(v[g][r][3])); }
; #pragma unroll
;         for (int c = 0; c < 4; ++c) { float m = mx[c]; m = fmaxf(m, __shfl_xor(m, 8)); m = fmaxf(m, __shfl_xor(m, 16)); m = fmaxf(m, __shfl_xor(m, 32)); mx[c] = m; }
;         if (tid == 0) MISC[2] = nxt;
;         if (kr == 0) *(LAS f32x4*)(smax + wave * 32 + 4 * n4) = mx;
.LBB0_1748:
	s_waitcnt vmcnt(10)
	v_max3_f32 v130, |v2|, 0, |v6|
	s_waitcnt vmcnt(8)
	v_max3_f32 v130, v130, |v10|, |v14|
	s_waitcnt vmcnt(26)
	v_max3_f32 v130, v130, |v18|, |v22|
	s_waitcnt vmcnt(24)
	v_max3_f32 v130, v130, |v26|, |v30|
	s_waitcnt vmcnt(22)
	v_max3_f32 v130, v130, |v34|, |v38|
	s_waitcnt vmcnt(20)
	v_max3_f32 v130, v130, |v42|, |v46|
	v_max3_f32 v131, |v3|, 0, |v7|
	s_waitcnt vmcnt(18)
	v_max3_f32 v130, v130, |v50|, |v54|
	v_max3_f32 v132, |v4|, 0, |v8|
	v_max3_f32 v131, v131, |v11|, |v15|
	s_waitcnt vmcnt(16)
	v_max3_f32 v130, v130, |v58|, |v62|
	v_max3_f32 v132, v132, |v12|, |v16|
	v_max3_f32 v131, v131, |v19|, |v23|
	s_waitcnt vmcnt(14)
	v_max3_f32 v130, v130, |v66|, |v70|
	v_max3_f32 v132, v132, |v20|, |v24|
	v_max3_f32 v131, v131, |v27|, |v31|
	s_waitcnt vmcnt(12)
	v_max3_f32 v130, v130, |v74|, |v78|
	v_max3_f32 v132, v132, |v28|, |v32|
	v_max3_f32 v131, v131, |v35|, |v39|
	s_waitcnt vmcnt(10)
	v_max3_f32 v130, v130, |v82|, |v86|
	v_max3_f32 v132, v132, |v36|, |v40|
	v_max3_f32 v131, v131, |v43|, |v47|
	s_waitcnt vmcnt(8)
	v_max3_f32 v130, v130, |v90|, |v94|
	v_max3_f32 v132, v132, |v44|, |v48|
	v_max3_f32 v131, v131, |v51|, |v55|
	s_waitcnt vmcnt(6)
	v_max3_f32 v130, v130, |v98|, |v102|
	v_max3_f32 v133, |v5|, 0, |v9|
	v_max3_f32 v132, v132, |v52|, |v56|
	v_max3_f32 v131, v131, |v59|, |v63|
	s_waitcnt vmcnt(4)
	v_max3_f32 v130, v130, |v106|, |v110|
	v_max3_f32 v133, v133, |v13|, |v17|
	v_max3_f32 v132, v132, |v60|, |v64|
	v_max3_f32 v131, v131, |v67|, |v71|
	s_waitcnt vmcnt(2)
	v_max3_f32 v130, v130, |v114|, |v118|
	v_max3_f32 v133, v133, |v21|, |v25|
	v_max3_f32 v132, v132, |v68|, |v72|
	v_max3_f32 v131, v131, |v75|, |v79|
	s_waitcnt vmcnt(0)
	v_max3_f32 v130, v130, |v122|, |v126|
	v_max3_f32 v133, v133, |v29|, |v33|
	v_max3_f32 v132, v132, |v76|, |v80|
	v_max3_f32 v131, v131, |v83|, |v87|
	v_max3_f32 v133, v133, |v37|, |v41|
	v_max3_f32 v132, v132, |v84|, |v88|
	v_max3_f32 v131, v131, |v91|, |v95|
	v_max3_f32 v133, v133, |v45|, |v49|
	v_max3_f32 v132, v132, |v92|, |v96|
	v_max3_f32 v131, v131, |v99|, |v103|
	v_max3_f32 v133, v133, |v53|, |v57|
	v_max3_f32 v132, v132, |v100|, |v104|
	v_max3_f32 v131, v131, |v107|, |v111|
	v_max3_f32 v133, v133, |v61|, |v65|
	v_max3_f32 v132, v132, |v108|, |v112|
	v_max3_f32 v131, v131, |v115|, |v119|
	v_max3_f32 v133, v133, |v69|, |v73|
	v_max3_f32 v132, v132, |v116|, |v120|
	v_max3_f32 v131, v131, |v123|, |v127|
	v_max3_f32 v133, v133, |v77|, |v81|
	v_max3_f32 v135, v132, |v124|, |v128|
	v_max3_f32 v133, v133, |v85|, |v89|
	v_max3_f32 v133, v133, |v93|, |v97|
	v_max3_f32 v133, v133, |v101|, |v105|
	v_max3_f32 v133, v133, |v109|, |v113|
	v_max3_f32 v133, v133, |v117|, |v121|
	v_max3_f32 v133, v133, |v125|, |v129|
	v_mov_b32_e32 v132, v135
	s_nop 1
	v_max_f32_dpp v130, v130, v130 row_ror:8 row_mask:0xf bank_mask:0xf
	v_max_f32_dpp v131, v131, v131 row_ror:8 row_mask:0xf bank_mask:0xf
	v_max_f32_dpp v132, v132, v132 row_ror:8 row_mask:0xf bank_mask:0xf
	v_max_f32_dpp v133, v133, v133 row_ror:8 row_mask:0xf bank_mask:0xf
	v_mov_b32_e32 v134, v130
	v_mov_b32_e32 v136, v131
	v_mov_b32_e32 v137, v132
	v_mov_b32_e32 v138, v133
	s_nop 1
	v_permlane16_swap_b32 v130, v134
	v_permlane16_swap_b32 v131, v136
	v_permlane16_swap_b32 v132, v137
	v_permlane16_swap_b32 v133, v138
	v_max_f32_e32 v130, v130, v134
	v_max_f32_e32 v131, v131, v136
	v_max_f32_e32 v132, v132, v137
	v_max_f32_e32 v133, v133, v138
	v_mov_b32_e32 v134, v130
	v_mov_b32_e32 v136, v131
	v_mov_b32_e32 v137, v132
	v_mov_b32_e32 v138, v133
	s_nop 1
	v_permlane32_swap_b32 v130, v134
	v_permlane32_swap_b32 v131, v136
	v_permlane32_swap_b32 v132, v137
	v_permlane32_swap_b32 v133, v138
	v_max_f32_e32 v130, v130, v134
	v_max_f32_e32 v131, v131, v136
	v_max_f32_e32 v132, v132, v137
	v_max_f32_e32 v133, v133, v138
	s_and_saveexec_b64 s[6:7], s[40:41]
	v_add_u32_e32 v1, 0x1c8, v201
	v_cmp_lt_i32_e32 vcc, 0, v163
	v_mov_b32_e32 v201, 0x1800
	s_and_b64 exec, exec, vcc
	v_mov_b32_e32 v203, 1
	global_atomic_add v201, v171, v203, s[20:21] sc0
	s_and_b64 exec, s[6:7], s[40:41]
	v_add_u32_e32 v163, -1, v163
	v_mov_b32_e32 v138, s3
	ds_write_b32 v138, v1
	s_or_b64 exec, exec, s[6:7]
	s_and_saveexec_b64 s[6:7], s[4:5]
	s_cbranch_execz .LBB0_1758
	v_add_u32_e32 v1, s42, v173
	ds_write_b128 v1, v[130:133]
